# per-batch arrival counters, faster poll, first-attempt upart loads L2-cacheable (NaN tags validate)
# speedup vs baseline: 1.0349x; 1.0349x over previous
.LBB1_18:
	s_or_b64 exec, exec, s[0:1]
	v_cmp_eq_u32_e32 vcc, 0, v0
	s_waitcnt lgkmcnt(0)
	s_and_saveexec_b64 s[0:1], vcc
	s_cbranch_execz .LBB1_21
	s_mov_b64 s[20:21], exec
	v_mbcnt_lo_u32_b32 v66, s20, 0
	v_mbcnt_hi_u32_b32 v66, s21, v66
	v_cmp_eq_u32_e32 vcc, 0, v66
	s_and_b64 s[38:39], exec, vcc
	s_mov_b64 exec, s[38:39]
	s_cbranch_execz .LBB1_21
	s_lshl_b32 s2, s43, 8
	s_and_b32 s2, s2, 0x700
	s_bcnt1_i32_b64 s20, s[20:21]
	v_mov_b32_e32 v66, s2
	v_mov_b32_e32 v67, s20
	global_atomic_add v66, v67, s[6:7]
.LBB1_21:
	s_or_b64 exec, exec, s[0:1]
	v_lshlrev_b32_e32 v73, 16, v225
	v_lshlrev_b32_e32 v84, 14, v224
	v_or3_b32 v66, v73, v213, v84
	v_lshlrev_b32_e32 v210, 2, v0
	v_mov_b32_e32 v211, 0
	ds_write_b128 v66, v[2:5]
	ds_write_b128 v66, v[6:9] offset:1024
	ds_write_b128 v66, v[10:13] offset:2048
	ds_write_b128 v66, v[14:17] offset:3072
	ds_write_b128 v66, v[34:37] offset:4096
	ds_write_b128 v66, v[38:41] offset:5120
	ds_write_b128 v66, v[42:45] offset:6144
	ds_write_b128 v66, v[46:49] offset:7168
	ds_write_b128 v66, v[50:53] offset:8192
	ds_write_b128 v66, v[54:57] offset:9216
	ds_write_b128 v66, v[58:61] offset:10240
	ds_write_b128 v66, v[62:65] offset:11264
	ds_write_b128 v66, v[18:21] offset:12288
	ds_write_b128 v66, v[22:25] offset:13312
	ds_write_b128 v66, v[26:29] offset:14336
	ds_write_b128 v66, v[30:33] offset:15360
	v_lshl_add_u64 v[66:67], s[18:19], 0, v[210:211]
	s_movk_i32 s0, 0x1000
	v_add_co_u32_e32 v68, vcc, s0, v66
	s_movk_i32 s0, 0x2000
	s_nop 0
	v_addc_co_u32_e32 v69, vcc, 0, v67, vcc
	v_add_co_u32_e32 v66, vcc, s0, v66
	s_waitcnt lgkmcnt(0)
	s_barrier
	global_load_dword v239, v210, s[18:19]
	global_load_dword v240, v210, s[18:19] offset:2048
	v_addc_co_u32_e32 v67, vcc, 0, v67, vcc
	global_load_dword v241, v[68:69], off offset:2048
	global_load_dword v242, v[66:67], off offset:-4096
	global_load_dword v243, v[66:67], off
	v_min_u32_e32 v66, 19, v212
	v_add_u32_e32 v66, s3, v66
	v_and_b32_e32 v238, 0x7f, v0
	v_ashrrev_i32_e32 v67, 31, v66
	v_lshlrev_b32_e32 v226, 2, v238
	v_lshl_add_u64 v[66:67], v[66:67], 2, s[22:23]
	global_load_dword v237, v226, s[30:31]
	global_load_dword v234, v226, s[12:13]
	global_load_dword v235, v226, s[28:29]
	global_load_dword v85, v[66:67], off
	v_cmp_gt_u32_e64 s[0:1], 20, v0
	v_lshrrev_b32_e32 v227, 7, v0
	v_lshrrev_b32_e32 v236, 5, v0
	v_cndmask_b32_e64 v66, 19, v0, s[0:1]
	v_lshlrev_b32_e32 v66, 2, v66
	global_load_dword v233, v66, s[26:27]
	v_mad_u32_u24 v66, v227, 5, s3
	v_lshl_or_b32 v66, v66, 7, v238
	v_add_u32_e32 v68, 0x80, v66
	v_ashrrev_i32_e32 v69, 31, v68
	v_lshl_add_u64 v[76:77], v[68:69], 2, s[16:17]
	v_add_u32_e32 v68, 0x100, v66
	v_ashrrev_i32_e32 v67, 31, v66
	v_ashrrev_i32_e32 v69, 31, v68
	v_lshl_add_u64 v[74:75], v[66:67], 2, s[16:17]
	v_lshl_add_u64 v[78:79], v[68:69], 2, s[16:17]
	v_add_u32_e32 v68, 0x180, v66
	v_add_u32_e32 v66, 0x200, v66
	v_ashrrev_i32_e32 v67, 31, v66
	v_ashrrev_i32_e32 v69, 31, v68
	v_lshl_add_u64 v[66:67], v[66:67], 2, s[16:17]
	v_lshl_add_u64 v[80:81], v[68:69], 2, s[16:17]
	global_load_dword v68, v[74:75], off
	global_load_dword v69, v[76:77], off
	global_load_dword v70, v[78:79], off
	global_load_dword v71, v[80:81], off
	global_load_dword v72, v[66:67], off
	v_lshlrev_b32_e32 v66, 4, v214
	v_mov_b32_e32 v67, v211
	v_lshl_add_u64 v[74:75], s[36:37], 0, v[66:67]
	v_lshlrev_b32_e32 v76, 12, v236
	v_mov_b32_e32 v77, v211
	v_lshl_add_u64 v[66:67], s[34:35], 0, v[66:67]
	v_lshl_add_u64 v[74:75], v[74:75], 0, v[76:77]
	v_lshl_add_u64 v[66:67], v[66:67], 0, v[76:77]
	global_load_dwordx4 v[206:209], v[74:75], off
	global_load_dwordx4 v[198:201], v[74:75], off offset:512
	global_load_dwordx4 v[202:205], v[66:67], off
	global_load_dwordx4 v[194:197], v[66:67], off offset:512
	global_load_dwordx4 v[190:193], v[74:75], off offset:1024
	global_load_dwordx4 v[182:185], v[74:75], off offset:1536
	global_load_dwordx4 v[186:189], v[66:67], off offset:1024
	global_load_dwordx4 v[178:181], v[66:67], off offset:1536
	global_load_dwordx4 v[174:177], v[74:75], off offset:2048
	global_load_dwordx4 v[166:169], v[74:75], off offset:2560
	global_load_dwordx4 v[170:173], v[66:67], off offset:2048
	global_load_dwordx4 v[162:165], v[66:67], off offset:2560
	global_load_dwordx4 v[158:161], v[74:75], off offset:3072
	global_load_dwordx4 v[150:153], v[74:75], off offset:3584
	global_load_dwordx4 v[154:157], v[66:67], off offset:3072
	global_load_dwordx4 v[146:149], v[66:67], off offset:3584
	v_mov_b32_e32 v66, 0xc8
	v_cmp_gt_u32_e32 vcc, 20, v212
	v_xor_b32_e32 v73, 0x10000, v73
	v_or3_b32 v73, v73, v213, v84
	ds_read_b128 v[142:145], v73
	ds_read_b128 v[138:141], v73 offset:1024
	ds_read_b128 v[134:137], v73 offset:2048
	ds_read_b128 v[130:133], v73 offset:3072
	ds_read_b128 v[126:129], v73 offset:4096
	ds_read_b128 v[122:125], v73 offset:5120
	ds_read_b128 v[118:121], v73 offset:6144
	ds_read_b128 v[114:117], v73 offset:7168
	ds_read_b128 v[110:113], v73 offset:8192
	ds_read_b128 v[106:109], v73 offset:9216
	ds_read_b128 v[98:101], v73 offset:10240
	ds_read_b128 v[90:93], v73 offset:11264
	s_waitcnt vmcnt(22)
	v_med3_i32 v66, v85, 0, v66
	v_cndmask_b32_e32 v66, 0, v66, vcc
	ds_bpermute_b32 v67, v232, v66
	s_waitcnt lgkmcnt(0)
	v_add_u32_e32 v66, v67, v66
	ds_bpermute_b32 v67, v231, v66
	s_waitcnt lgkmcnt(0)
	v_add_u32_e32 v66, v66, v67
	ds_bpermute_b32 v67, v230, v66
	s_waitcnt lgkmcnt(0)
	v_add_u32_e32 v66, v66, v67
	ds_bpermute_b32 v67, v229, v66
	s_waitcnt lgkmcnt(0)
	v_add_u32_e32 v66, v66, v67
	ds_bpermute_b32 v67, v228, v66
	s_waitcnt lgkmcnt(0)
	v_add_u32_e32 v66, v66, v67
	v_xor_b32_e32 v67, 32, v82
	v_cmp_lt_i32_e32 vcc, v67, v83
	s_nop 1
	v_cndmask_b32_e32 v67, v82, v67, vcc
	v_lshlrev_b32_e32 v67, 2, v67
	ds_bpermute_b32 v67, v67, v66
	ds_read_b128 v[102:105], v73 offset:12288
	ds_read_b128 v[94:97], v73 offset:13312
	ds_read_b128 v[86:89], v73 offset:14336
	ds_read_b128 v[82:85], v73 offset:15360
	s_load_dword s18, s[8:9], 0x0
	v_cmp_gt_u32_e32 vcc, 64, v0
	s_waitcnt lgkmcnt(0)
	v_add_u32_e32 v66, v66, v67
	v_cvt_f32_i32_e32 v73, v66
	s_barrier
	s_and_saveexec_b64 s[8:9], vcc
	s_cbranch_execz .LBB1_40
	v_mov_b32_e32 v66, s43
	v_lshlrev_b32_e32 v66, 8, v66
	v_mov_b32_e32 v67, v211
	v_cmp_gt_u32_e64 s[2:3], 8, v212
	v_lshl_add_u64 v[66:67], s[6:7], 0, v[66:67]
	s_mov_b32 s19, -5
	s_branch .LBB1_24

.LBB1_26:
	s_or_b64 exec, exec, s[12:13]
	v_cndmask_b32_e64 v74, 0, 1, s[16:17]
	v_cmp_ne_u32_e32 vcc, 0, v74
	s_cmp_eq_u64 vcc, exec
	s_cbranch_scc1 .LBB1_23
	s_mov_b64 s[16:17], -1
	s_sleep 3
	s_and_saveexec_b64 s[12:13], s[2:3]
	s_cbranch_execz .LBB1_29
	global_load_dword v74, v[66:67], off sc1
	s_waitcnt vmcnt(0)
	v_cmp_lt_u32_e32 vcc, 31, v74
	s_orn2_b64 s[16:17], vcc, exec

.LBB1_38:
	s_or_b64 exec, exec, s[12:13]
	v_cndmask_b32_e64 v74, 0, 1, s[16:17]
	v_cmp_ne_u32_e32 vcc, 0, v74
	s_cmp_eq_u64 vcc, exec
	s_cbranch_scc1 .LBB1_23
	s_add_i32 s19, s19, 5
	s_cmp_gt_u32 s19, 0x3ffffb
	s_cselect_b64 s[6:7], -1, 0
	s_sleep 3
	s_branch .LBB1_23
.LBB1_40:
	s_or_b64 exec, exec, s[8:9]
	s_waitcnt vmcnt(20)
	v_add_f32_e32 v66, 0, v68
	s_waitcnt vmcnt(19)
	v_add_f32_e32 v66, v66, v69
	s_waitcnt vmcnt(18)
	v_add_f32_e32 v66, v66, v70
	s_waitcnt vmcnt(17)
	v_add_f32_e32 v66, v66, v71
	s_waitcnt vmcnt(16)
	v_add_f32_e32 v246, v66, v72
	v_lshlrev_b32_e32 v66, 11, v227
	v_lshl_or_b32 v68, s43, 13, v66
	v_or_b32_e32 v66, v68, v238
	v_or_b32_e32 v77, v68, v0
	v_ashrrev_i32_e32 v67, 31, v66
	v_or_b32_e32 v68, 0x380, v77
	v_lshl_add_u64 v[66:67], v[66:67], 2, s[4:5]
	v_ashrrev_i32_e32 v69, 31, v68
	v_max_f32_e32 v245, 1.0, v73
	s_barrier
	global_load_dword v70, v[66:67], off
	global_load_dword v71, v[66:67], off offset:512
	global_load_dword v72, v[66:67], off offset:1024
	global_load_dword v73, v[66:67], off offset:1536
	global_load_dword v74, v[66:67], off offset:2048
	global_load_dword v75, v[66:67], off offset:2560
	global_load_dword v76, v[66:67], off offset:3072
	v_lshl_add_u64 v[68:69], v[68:69], 2, s[4:5]
	global_load_dword v68, v[68:69], off
	s_movk_i32 s2, 0x1000
	v_add_co_u32_e32 v66, vcc, s2, v66
	v_lshlrev_b32_e32 v211, 2, v214
	s_nop 0
	v_addc_co_u32_e32 v67, vcc, 0, v67, vcc
	global_load_dword v69, v[66:67], off
	global_load_dword v78, v[66:67], off offset:512
	global_load_dword v79, v[66:67], off offset:1024
	global_load_dword v80, v[66:67], off offset:1536
	global_load_dword v81, v[66:67], off offset:2048
	global_load_dword v214, v[66:67], off offset:2560
	global_load_dword v215, v[66:67], off offset:3072
	v_or_b32_e32 v66, 0x780, v77
	v_ashrrev_i32_e32 v67, 31, v66
	s_mov_b32 s2, 0xccccccd
	v_lshl_add_u64 v[66:67], v[66:67], 2, s[4:5]
	v_mul_hi_u32 v244, v0, s2
	global_load_dword v247, v[66:67], off
	v_mul_u32_u24_e32 v66, 20, v244
	s_movk_i32 s2, 0x140
	v_sub_u32_e32 v77, v0, v66
	v_cmp_gt_u32_e64 s[2:3], s2, v0
	v_lshlrev_b32_e32 v66, 3, v244
	v_mov_b32_e32 v67, 0x78
	v_cndmask_b32_e64 v216, v67, v66, s[2:3]
	v_mul_u32_u24_e32 v66, 20, v216
	v_or_b32_e32 v212, v66, v77
	v_mov_b32_e32 v213, 0
	v_lshl_add_u64 v[66:67], v[212:213], 2, s[14:15]
	v_mad_u32_u24 v212, v216, 20, v77
	global_load_dword v220, v[66:67], off
	v_lshl_add_u64 v[66:67], v[212:213], 2, s[14:15]
	global_load_dword v221, v[66:67], off offset:80
	global_load_dword v222, v[66:67], off offset:160
	global_load_dword v223, v[66:67], off offset:240
	global_load_dword v218, v[66:67], off offset:320
	global_load_dword v219, v[66:67], off offset:400
	global_load_dword v216, v[66:67], off offset:480
	global_load_dword v217, v[66:67], off offset:560
	v_lshlrev_b32_e32 v212, 7, v224
	s_movk_i32 s4, 0x180
	s_waitcnt vmcnt(23)
	v_add_f32_e32 v66, 0, v70
	s_waitcnt vmcnt(22)
	v_add_f32_e32 v66, v66, v71
	s_waitcnt vmcnt(21)
	v_add_f32_e32 v66, v66, v72
	s_waitcnt vmcnt(20)
	v_add_f32_e32 v66, v66, v73
	s_waitcnt vmcnt(19)
	v_add_f32_e32 v66, v66, v74
	s_waitcnt vmcnt(18)
	v_add_f32_e32 v66, v66, v75
	s_waitcnt vmcnt(17)
	v_add_f32_e32 v66, v66, v76
	s_waitcnt vmcnt(16)
	v_add_f32_e32 v66, v66, v68
	s_waitcnt vmcnt(15)
	v_add_f32_e32 v66, v66, v69
	s_waitcnt vmcnt(14)
	v_add_f32_e32 v66, v66, v78
	s_waitcnt vmcnt(13)
	v_add_f32_e32 v66, v66, v79
	s_waitcnt vmcnt(12)
	v_add_f32_e32 v66, v66, v80
	s_waitcnt vmcnt(11)
	v_add_f32_e32 v66, v66, v81
	s_waitcnt vmcnt(10)
	v_add_f32_e32 v66, v66, v214
	s_waitcnt vmcnt(9)
	v_add_f32_e32 v248, v66, v215
	v_lshl_add_u64 v[66:67], s[24:25], 0, v[212:213]
	v_lshlrev_b32_e32 v214, 4, v1
	v_mov_b32_e32 v215, v213
	v_lshl_add_u64 v[78:79], v[66:67], 0, v[214:215]
	global_load_dwordx4 v[66:69], v[78:79], off
	global_load_dwordx4 v[70:73], v[78:79], off offset:32
	global_load_dwordx4 v[74:77], v[78:79], off offset:64
	s_nop 0
	global_load_dwordx4 v[78:81], v[78:79], off offset:96
	s_waitcnt vmcnt(12)
	v_add_f32_e32 v215, v248, v247
